# redundant MFMA->VALU drain nops removed before the P1/P5/P6 epilogues (first accumulator read is >20 instructions later)
# baseline (speedup 1.0000x reference)
; #define PG8_STAGE(bufoff, base, uoff, voff) do { _Pragma("unroll") for (int _i = 0; _i < 2; ++_i) \
;         __builtin_amdgcn_raw_ptr_buffer_load_lds((base), (PG8_LAS void*)(lds + (bufoff) + ldsw + _i * 8192), 16, (int)(voff)[_i], (int)(uoff), 0, 0); } while (0)
; #define PG8_LDA(dst, b, h) do { _Pragma("unroll") for (int m = 0; m < 4; ++m) _Pragma("unroll") for (int k = 0; k < 2; ++k) dst[m][k] = *(const PG8_LAS bf16x8*)(lds + PG8_SA(b, h) + aoff + m * 2048 + k * 1024); } while (0)
; #define PG8_WAIT_V(n) asm volatile("s_waitcnt vmcnt(" #n ")" ::: "memory")
; #define PG8_WAIT_L(n) asm volatile("s_waitcnt lgkmcnt(" #n ")" ::: "memory")
; #define PG8_BAR __builtin_amdgcn_s_barrier()
; #define PG8_SCHED __builtin_amdgcn_sched_barrier(0)
; template <class Epi, class Sched, bool GATHER, int MODE>
; __device__ __forceinline__ void gemm_phase(PG8_LAS unsigned char* lds, PG8_LAS unsigned* scr, const Gemm g, const Sched& S, const Epi& E, int tid_in) {
;     ...
;             PG8_LDA(At, 1, 1); PG8_STAGE(PG8_SB(1, 0), baseB, b3, voffB); PG8_STAGE(PG8_SB(1, 1), baseB, b3 + hstep, voffB); PG8_STAGE(PG8_SA(1, 0), baseA, a3, s0);
;             PG8_WAIT_V(8); PG8_WAIT_L(0); PG8_BAR; PG8_MMA(1, 0, At, B0); PG8_MMA(1, 1, At, B1); PG8_BAR; PG8_SCHED;
;         }
;         asm volatile("s_nop 15\n\ts_nop 7" ::: "memory");
.Lp1_nostash:
	s_mov_b32 m0, s58
	s_add_i32 s79, s78, 0x80
	ds_read_b128 v[204:207], v201 offset:49152
	ds_read_b128 v[208:211], v201 offset:50176
	ds_read_b128 v[212:215], v201 offset:51200
	ds_read_b128 v[216:219], v201 offset:52224
	ds_read_b128 v[220:223], v201 offset:53248
	ds_read_b128 v[224:227], v201 offset:54272
	ds_read_b128 v[228:231], v201 offset:55296
	ds_read_b128 v[232:235], v201 offset:56320
	buffer_load_dwordx4 v168, s[40:43], s79 offen lds
	s_mov_b32 m0, s59
	s_add_i32 s78, s78, 0x20080
	buffer_load_dwordx4 v181, s[40:43], s79 offen lds
	s_mov_b32 m0, s62
	s_nop 0
	buffer_load_dwordx4 v168, s[40:43], s78 offen lds
	s_mov_b32 m0, s63
	s_nop 0
	buffer_load_dwordx4 v181, s[40:43], s78 offen lds
	s_mov_b32 m0, s60
	s_nop 0
	buffer_load_dwordx4 v167, s[4:7], s77 offen lds
	s_mov_b32 m0, s61
	s_nop 0
	buffer_load_dwordx4 v180, s[4:7], s77 offen lds
	s_waitcnt vmcnt(8)
	s_waitcnt lgkmcnt(0)
	s_barrier
	s_setprio 1
	s_waitcnt lgkmcnt(7)
	v_mfma_i32_16x16x64_i8 v[84:87], v[128:131], v[204:207], v[84:87]
	s_waitcnt lgkmcnt(6)
	v_mfma_i32_16x16x64_i8 v[84:87], v[132:135], v[208:211], v[84:87]
	v_mfma_i32_16x16x64_i8 v[80:83], v[136:139], v[204:207], v[80:83]
	s_nop 0
	v_mfma_i32_16x16x64_i8 v[80:83], v[140:143], v[208:211], v[80:83]
	s_waitcnt lgkmcnt(5)
	v_mfma_i32_16x16x64_i8 v[52:55], v[128:131], v[212:215], v[52:55]
	s_waitcnt lgkmcnt(4)
	v_mfma_i32_16x16x64_i8 v[52:55], v[132:135], v[216:219], v[52:55]
	v_mfma_i32_16x16x64_i8 v[48:51], v[136:139], v[212:215], v[48:51]
	s_nop 0
	v_mfma_i32_16x16x64_i8 v[48:51], v[140:143], v[216:219], v[48:51]
	s_waitcnt lgkmcnt(3)
	v_mfma_i32_16x16x64_i8 v[20:23], v[128:131], v[220:223], v[20:23]
	s_waitcnt lgkmcnt(2)
	v_mfma_i32_16x16x64_i8 v[20:23], v[132:135], v[224:227], v[20:23]
	v_mfma_i32_16x16x64_i8 v[16:19], v[136:139], v[220:223], v[16:19]
	s_nop 0
	v_mfma_i32_16x16x64_i8 v[16:19], v[140:143], v[224:227], v[16:19]
	s_waitcnt lgkmcnt(1)
	v_mfma_i32_16x16x64_i8 v[8:11], v[128:131], v[228:231], v[8:11]
	s_waitcnt lgkmcnt(0)
	v_mfma_i32_16x16x64_i8 v[8:11], v[132:135], v[232:235], v[8:11]
	v_mfma_i32_16x16x64_i8 v[0:3], v[136:139], v[228:231], v[0:3]
	s_nop 0
	v_mfma_i32_16x16x64_i8 v[0:3], v[140:143], v[232:235], v[0:3]
	s_setprio 0
	s_setprio 1
	v_mfma_i32_16x16x64_i8 v[96:99], v[144:147], v[204:207], v[96:99]
	s_nop 0
	v_mfma_i32_16x16x64_i8 v[96:99], v[150:153], v[208:211], v[96:99]
	v_mfma_i32_16x16x64_i8 v[92:95], v[154:157], v[204:207], v[92:95]
	s_nop 0
	v_mfma_i32_16x16x64_i8 v[92:95], v[158:161], v[208:211], v[92:95]
	v_mfma_i32_16x16x64_i8 v[72:75], v[144:147], v[212:215], v[72:75]
	s_nop 0
	v_mfma_i32_16x16x64_i8 v[72:75], v[150:153], v[216:219], v[72:75]
	v_mfma_i32_16x16x64_i8 v[64:67], v[154:157], v[212:215], v[64:67]
	s_nop 0
	v_mfma_i32_16x16x64_i8 v[64:67], v[158:161], v[216:219], v[64:67]
	v_mfma_i32_16x16x64_i8 v[40:43], v[144:147], v[220:223], v[40:43]
	s_nop 0
	v_mfma_i32_16x16x64_i8 v[40:43], v[150:153], v[224:227], v[40:43]
	v_mfma_i32_16x16x64_i8 v[36:39], v[154:157], v[220:223], v[36:39]
	s_nop 0
	v_mfma_i32_16x16x64_i8 v[36:39], v[158:161], v[224:227], v[36:39]
	v_mfma_i32_16x16x64_i8 v[12:15], v[144:147], v[228:231], v[12:15]
	s_nop 0
	v_mfma_i32_16x16x64_i8 v[12:15], v[150:153], v[232:235], v[12:15]
	v_mfma_i32_16x16x64_i8 v[4:7], v[154:157], v[228:231], v[4:7]
	s_nop 0
	v_mfma_i32_16x16x64_i8 v[4:7], v[158:161], v[232:235], v[4:7]
	s_setprio 0
	s_barrier
	s_cmp_gt_u32 s76, 5
	s_mov_b32 s77, s76
	s_cbranch_scc0 .LBB0_350
	s_nop 0

; template <class Epi, class Sched, bool GATHER, int MODE>
; __device__ __forceinline__ void gemm_phase(PG8_LAS unsigned char* lds, PG8_LAS unsigned* scr, const Gemm g, const Sched& S, const Epi& E, int tid_in) {
;     ...
;         }
;         asm volatile("s_nop 15\n\ts_nop 7" ::: "memory");
.LBB0_805:
	s_nop 0

; #define PG8_STAGE(bufoff, base, uoff, voff) do { _Pragma("unroll") for (int _i = 0; _i < 2; ++_i) \
;         __builtin_amdgcn_raw_ptr_buffer_load_lds((base), (PG8_LAS void*)(lds + (bufoff) + ldsw + _i * 8192), 16, (int)(voff)[_i], (int)(uoff), 0, 0); } while (0)
; #define PG8_LDA(dst, b, h) do { _Pragma("unroll") for (int m = 0; m < 4; ++m) _Pragma("unroll") for (int k = 0; k < 2; ++k) dst[m][k] = *(const PG8_LAS bf16x8*)(lds + PG8_SA(b, h) + aoff + m * 2048 + k * 1024); } while (0)
; #define PG8_WAIT_V(n) asm volatile("s_waitcnt vmcnt(" #n ")" ::: "memory")
; #define PG8_WAIT_L(n) asm volatile("s_waitcnt lgkmcnt(" #n ")" ::: "memory")
; #define PG8_BAR __builtin_amdgcn_s_barrier()
; #define PG8_SCHED __builtin_amdgcn_sched_barrier(0)
; template <class Epi, class Sched, bool GATHER, int MODE>
; __device__ __forceinline__ void gemm_phase(PG8_LAS unsigned char* lds, PG8_LAS unsigned* scr, const Gemm g, const Sched& S, const Epi& E, int tid_in) {
;     ...
;             PG8_LDA(At, 1, 1); PG8_STAGE(PG8_SB(1, 0), baseB, b3, voffB); PG8_STAGE(PG8_SB(1, 1), baseB, b3 + hstep, voffB); PG8_STAGE(PG8_SA(1, 0), baseA, a3, s0);
;             PG8_WAIT_V(8); PG8_WAIT_L(0); PG8_BAR; PG8_MMA(1, 0, At, B0); PG8_MMA(1, 1, At, B1); PG8_BAR; PG8_SCHED;
;         }
;         asm volatile("s_nop 15\n\ts_nop 7" ::: "memory");
.Lp6_nostash:
	s_mov_b32 m0, s60
	s_add_i32 s83, s82, 0x80
	ds_read_b128 v[210:213], v206 offset:49152
	ds_read_b128 v[214:217], v206 offset:50176
	ds_read_b128 v[218:221], v206 offset:51200
	ds_read_b128 v[222:225], v206 offset:52224
	ds_read_b128 v[226:229], v206 offset:53248
	ds_read_b128 v[230:233], v206 offset:54272
	ds_read_b128 v[242:245], v206 offset:55296
	ds_read_b128 v[246:249], v206 offset:56320
	buffer_load_dwordx4 v201, s[40:43], s83 offen lds
	s_mov_b32 m0, s61
	s_add_i32 s82, s82, 0x20080
	buffer_load_dwordx4 v203, s[40:43], s83 offen lds
	s_mov_b32 m0, s64
	s_nop 0
	buffer_load_dwordx4 v201, s[40:43], s82 offen lds
	s_mov_b32 m0, s65
	s_nop 0
	buffer_load_dwordx4 v203, s[40:43], s82 offen lds
	s_mov_b32 m0, s62
	s_nop 0
	buffer_load_dwordx4 v181, s[4:7], s81 offen lds
	s_mov_b32 m0, s63
	s_nop 0
	buffer_load_dwordx4 v202, s[4:7], s81 offen lds
	s_waitcnt vmcnt(8)
	s_waitcnt lgkmcnt(0)
	s_barrier
	s_setprio 1
	s_waitcnt lgkmcnt(6)
	v_mfma_f32_16x16x128_f8f6f4 v[96:99], v[16:23], v[210:217], v[96:99]
	v_mfma_f32_16x16x128_f8f6f4 v[88:91], v[24:31], v[210:217], v[88:91]
	s_waitcnt lgkmcnt(4)
	v_mfma_f32_16x16x128_f8f6f4 v[84:87], v[16:23], v[218:225], v[84:87]
	v_mfma_f32_16x16x128_f8f6f4 v[80:83], v[24:31], v[218:225], v[80:83]
	s_waitcnt lgkmcnt(2)
	v_mfma_f32_16x16x128_f8f6f4 v[72:75], v[16:23], v[226:233], v[72:75]
	v_mfma_f32_16x16x128_f8f6f4 v[76:79], v[24:31], v[226:233], v[76:79]
	s_waitcnt lgkmcnt(0)
	v_mfma_f32_16x16x128_f8f6f4 v[68:71], v[16:23], v[242:249], v[68:71]
	v_mfma_f32_16x16x128_f8f6f4 v[64:67], v[24:31], v[242:249], v[64:67]
	s_setprio 0
	s_setprio 1
	v_mfma_f32_16x16x128_f8f6f4 v[100:103], v[8:15], v[210:217], v[100:103]
	v_mfma_f32_16x16x128_f8f6f4 v[92:95], v[0:7], v[210:217], v[92:95]
	v_mfma_f32_16x16x128_f8f6f4 v[60:63], v[8:15], v[218:225], v[60:63]
	v_mfma_f32_16x16x128_f8f6f4 v[56:59], v[0:7], v[218:225], v[56:59]
	v_mfma_f32_16x16x128_f8f6f4 v[48:51], v[8:15], v[226:233], v[48:51]
	v_mfma_f32_16x16x128_f8f6f4 v[52:55], v[0:7], v[226:233], v[52:55]
	v_mfma_f32_16x16x128_f8f6f4 v[44:47], v[8:15], v[242:249], v[44:47]
	v_mfma_f32_16x16x128_f8f6f4 v[40:43], v[0:7], v[242:249], v[40:43]
	s_setprio 0
	s_barrier
	s_cmp_gt_u32 s80, 5
	s_mov_b32 s81, s80
	s_cbranch_scc0 .LBB0_958
	s_nop 0
